# nt hint on MoE f32 weight loads + relaxed compiler vmcnt(0) drains before the GEMM K-loops
# speedup vs baseline: 1.0079x; 1.0000x over previous
.LBB0_1432:
	s_lshr_b32 s33, s2, 6
	s_lshl_b32 s3, s33, 1
	v_or_b32_e32 v2, s3, v193
	s_and_b32 s36, s33, 4
	s_and_b32 s37, s2, 0xc0
	v_and_or_b32 v3, v2, 3, s36
	s_lshr_b32 s36, s2, 1
	s_or_b32 s2, s37, 32
	v_bitop3_b32 v183, s2, v203, v198 bitop3:0xde
	s_or_b32 s2, s37, 0x100
	v_bitop3_b32 v181, s2, v203, v198 bitop3:0xde
	s_or_b32 s2, s37, 0x120
	s_lshl_b32 s38, s33, 10
	v_bitop3_b32 v172, s2, v203, v198 bitop3:0xde
	s_add_i32 s38, s38, 0
	s_mov_b32 s2, m0
	s_mov_b32 m0, s38
	s_nop 0
	global_load_lds_dwordx4 v34, s[18:19]
	s_mov_b32 m0, s2
	s_add_i32 s2, s38, 0x2000
	s_mov_b32 s39, m0
	s_mov_b32 m0, s2
	s_nop 0
	global_load_lds_dwordx4 v35, s[18:19]
	s_mov_b32 m0, s39
	s_add_i32 s2, s38, 0x4000
	s_mov_b32 s39, m0
	s_mov_b32 m0, s2
	s_nop 0
	global_load_lds_dwordx4 v36, s[18:19]
	s_mov_b32 m0, s39
	s_add_i32 s2, s38, 0x6000
	v_lshlrev_b32_e32 v2, 9, v2
	v_lshlrev_b32_e32 v3, 5, v3
	s_and_b32 s36, s36, 0x7fffff80
	s_mov_b32 s39, m0
	s_mov_b32 m0, s2
	s_nop 0
	global_load_lds_dwordx4 v37, s[18:19]
	s_mov_b32 m0, s39
	s_mul_i32 s2, s33, 0x5800
	v_bitop3_b32 v214, v3, v2, v194 bitop3:0xde
	v_or_b32_e32 v2, s36, v1
	s_mul_hi_u32 s39, s3, 0x2c00
	s_add_u32 s40, s59, s2
	s_waitcnt vmcnt(1)
	v_lshlrev_b32_e32 v38, 7, v2
	s_addc_u32 s41, s73, s39
	global_load_dwordx4 v[2:5], v199, s[40:41] nt
	s_add_i32 s40, s3, 16
	s_add_i32 s83, s2, 0x2c000
	s_mul_hi_u32 s84, s40, 0x2c00
	s_add_u32 s40, s59, s83
	s_addc_u32 s41, s73, s84
	global_load_dwordx4 v[6:9], v199, s[40:41] nt
	s_add_i32 s40, s3, 32
	s_add_i32 s85, s2, 0x58000
	s_mul_hi_u32 s86, s40, 0x2c00
	s_add_u32 s40, s59, s85
	s_addc_u32 s41, s73, s86
	global_load_dwordx4 v[10:13], v199, s[40:41] nt
	s_add_i32 s40, s3, 48
	s_add_i32 s87, s2, 0x84000
	s_mul_hi_u32 s88, s40, 0x2c00
	s_add_u32 s40, s59, s87
	s_addc_u32 s41, s73, s88
	global_load_dwordx4 v[14:17], v199, s[40:41] nt
	s_add_u32 s40, s74, s2
	s_addc_u32 s41, s75, s39
	global_load_dwordx4 v[18:21], v199, s[40:41] nt
	s_add_u32 s40, s74, s83
	s_addc_u32 s41, s75, s84
	global_load_dwordx4 v[22:25], v199, s[40:41] nt
	s_add_u32 s40, s74, s85
	s_addc_u32 s41, s75, s86
	global_load_dwordx4 v[26:29], v199, s[40:41] nt
	s_add_u32 s40, s74, s87
	s_addc_u32 s41, s75, s88
	global_load_dwordx4 v[30:33], v199, s[40:41] nt
	s_add_i32 s40, s38, 0x8000
	v_add_u32_e32 v39, 0x80, v34
	s_mov_b32 s41, m0
	s_mov_b32 m0, s40
	s_nop 0
	global_load_lds_dwordx4 v39, s[18:19]
	s_mov_b32 m0, s41
	v_add_u32_e32 v39, 0x80, v35
	s_add_i32 s40, s38, 0xa000
	s_mov_b32 s41, m0
	s_mov_b32 m0, s40
	s_nop 0
	global_load_lds_dwordx4 v39, s[18:19]
	s_mov_b32 m0, s41
	v_add_u32_e32 v39, 0x80, v36
	s_add_i32 s40, s38, 0xc000
	s_mov_b32 s41, m0
	s_mov_b32 m0, s40
	s_nop 0
	global_load_lds_dwordx4 v39, s[18:19]
	s_mov_b32 m0, s41
	v_add_u32_e32 v39, 0x80, v37
	s_add_i32 s40, s38, 0xe000
	s_mov_b32 s41, m0
	s_mov_b32 m0, s40
	s_nop 0
	global_load_lds_dwordx4 v39, s[18:19]
	s_mov_b32 m0, s41
	s_waitcnt vmcnt(4)
	v_add_u32_e32 v217, s52, v214
	v_cvt_pk_bf16_f32 v2, v2, v3
	v_cvt_pk_bf16_f32 v3, v4, v5
	v_cvt_pk_bf16_f32 v4, v6, v7
	v_cvt_pk_bf16_f32 v5, v8, v9
	v_or_b32_e32 v213, 0x100, v214
	ds_write2st64_b64 v217, v[2:3], v[4:5] offset1:16
	v_cvt_pk_bf16_f32 v2, v10, v11
	v_cvt_pk_bf16_f32 v3, v12, v13
	v_cvt_pk_bf16_f32 v4, v14, v15
	v_cvt_pk_bf16_f32 v5, v16, v17
	ds_write2st64_b64 v217, v[2:3], v[4:5] offset0:32 offset1:48
	v_cvt_pk_bf16_f32 v2, v18, v19
	v_cvt_pk_bf16_f32 v3, v20, v21
	v_add_u32_e32 v6, s52, v213
	v_cvt_pk_bf16_f32 v4, v22, v23
	v_cvt_pk_bf16_f32 v5, v24, v25
	s_add_i32 s40, s3, 64
	s_add_i32 s83, s2, 0xb0000
	ds_write2st64_b64 v6, v[2:3], v[4:5] offset1:16
	v_cvt_pk_bf16_f32 v2, v26, v27
	v_cvt_pk_bf16_f32 v3, v28, v29
	v_cvt_pk_bf16_f32 v4, v30, v31
	v_cvt_pk_bf16_f32 v5, v32, v33
	s_mul_hi_u32 s84, s40, 0x2c00
	s_add_u32 s40, s59, s83
	ds_write2st64_b64 v6, v[2:3], v[4:5] offset0:32 offset1:48
	s_addc_u32 s41, s73, s84
	global_load_dwordx4 v[30:33], v199, s[40:41] nt
	s_add_i32 s40, s3, 0x50
	s_add_i32 s85, s2, 0xdc000
	s_mul_hi_u32 s86, s40, 0x2c00
	s_add_u32 s40, s59, s85
	s_addc_u32 s41, s73, s86
	global_load_dwordx4 v[26:29], v199, s[40:41] nt
	s_add_i32 s40, s3, 0x60
	s_add_i32 s87, s2, 0x108000
	s_mul_hi_u32 s88, s40, 0x2c00
	s_add_u32 s40, s59, s87
	s_addc_u32 s41, s73, s88
	s_addk_i32 s3, 0x70
	s_add_i32 s89, s2, 0x134000
	global_load_dwordx4 v[22:25], v199, s[40:41] nt
	s_mul_hi_u32 s3, s3, 0x2c00
	s_add_u32 s40, s59, s89
	s_addc_u32 s41, s73, s3
	global_load_dwordx4 v[18:21], v199, s[40:41] nt
	s_add_u32 s40, s74, s83
	s_addc_u32 s41, s75, s84
	global_load_dwordx4 v[14:17], v199, s[40:41] nt
	s_add_u32 s40, s74, s85
	s_addc_u32 s41, s75, s86
	global_load_dwordx4 v[10:13], v199, s[40:41] nt
	s_add_u32 s40, s74, s87
	s_addc_u32 s41, s75, s88
	global_load_dwordx4 v[6:9], v199, s[40:41] nt
	s_add_u32 s40, s74, s89
	s_addc_u32 s41, s75, s3
	global_load_dwordx4 v[2:5], v199, s[40:41] nt
	s_mul_hi_u32 s3, s33, 0x5800
	s_add_u32 s40, s74, s2
	s_waitcnt lgkmcnt(0)
	s_barrier
	s_addc_u32 s41, s75, s3
	s_add_u32 s83, s59, s2
	v_add_u32_e32 v221, 0x100, v34
	v_mov_b32_e32 v34, 0
	v_bitop3_b32 v212, s37, v203, v198 bitop3:0xde
	v_or_b32_e32 v215, v38, v196
	s_mov_b32 s39, 0x8000
	v_or_b32_e32 v216, v38, v197
	s_addc_u32 s84, s73, s3
	v_add_u32_e32 v218, 0x100, v37
	v_add_u32_e32 v219, 0x100, v36
	v_add_u32_e32 v220, 0x100, v35
	s_mov_b32 s85, 0x10000
	s_mov_b32 s86, 0
	s_mov_b64 s[2:3], 0
	v_mov_b32_e32 v35, v34
	v_mov_b32_e32 v36, v34
	v_mov_b32_e32 v37, v34
	v_mov_b32_e32 v38, v34
	v_mov_b32_e32 v39, v34
	v_mov_b32_e32 v40, v34
	v_mov_b32_e32 v41, v34
	v_mov_b32_e32 v46, v34
	v_mov_b32_e32 v47, v34
	v_mov_b32_e32 v48, v34
	v_mov_b32_e32 v49, v34
	v_mov_b32_e32 v50, v34
	v_mov_b32_e32 v51, v34
	v_mov_b32_e32 v52, v34
	v_mov_b32_e32 v53, v34
	s_waitcnt vmcnt(12)
	v_mov_b32_e32 v42, v34
	v_mov_b32_e32 v43, v34
	v_mov_b32_e32 v44, v34
	v_mov_b32_e32 v45, v34
	v_mov_b32_e32 v54, v34
	v_mov_b32_e32 v55, v34
	v_mov_b32_e32 v56, v34
	v_mov_b32_e32 v57, v34
	v_mov_b32_e32 v58, v34
	v_mov_b32_e32 v59, v34
	v_mov_b32_e32 v60, v34
	v_mov_b32_e32 v61, v34
	v_mov_b32_e32 v62, v34
	v_mov_b32_e32 v63, v34
	v_mov_b32_e32 v64, v34
	v_mov_b32_e32 v65, v34
	v_mov_b32_e32 v66, v34
	v_mov_b32_e32 v67, v34
	v_mov_b32_e32 v68, v34
	v_mov_b32_e32 v69, v34
	v_mov_b32_e32 v70, v34
	v_mov_b32_e32 v71, v34
	v_mov_b32_e32 v72, v34
	v_mov_b32_e32 v73, v34
	v_mov_b32_e32 v74, v34
	v_mov_b32_e32 v75, v34
	v_mov_b32_e32 v76, v34
	v_mov_b32_e32 v77, v34
	v_mov_b32_e32 v78, v34
	v_mov_b32_e32 v79, v34
	v_mov_b32_e32 v80, v34
	v_mov_b32_e32 v81, v34
	v_mov_b32_e32 v82, v34
	v_mov_b32_e32 v83, v34
	v_mov_b32_e32 v84, v34
	v_mov_b32_e32 v85, v34
	v_mov_b32_e32 v86, v34
	v_mov_b32_e32 v87, v34
	v_mov_b32_e32 v88, v34
	v_mov_b32_e32 v89, v34
	v_mov_b32_e32 v90, v34
	v_mov_b32_e32 v91, v34
	v_mov_b32_e32 v92, v34
	v_mov_b32_e32 v93, v34
	v_mov_b32_e32 v94, v34
	v_mov_b32_e32 v95, v34
	v_mov_b32_e32 v96, v34
	v_mov_b32_e32 v97, v34
	v_mov_b32_e32 v98, v34
	v_mov_b32_e32 v99, v34
	v_mov_b32_e32 v100, v34
	v_mov_b32_e32 v101, v34
	v_mov_b32_e32 v102, v34
	v_mov_b32_e32 v103, v34
	v_mov_b32_e32 v104, v34
	v_mov_b32_e32 v105, v34
	v_mov_b32_e32 v106, v34
	v_mov_b32_e32 v107, v34
	v_mov_b32_e32 v108, v34
	v_mov_b32_e32 v109, v34
	v_mov_b32_e32 v110, v34
	v_mov_b32_e32 v111, v34
	v_mov_b32_e32 v112, v34
	v_mov_b32_e32 v113, v34
	v_mov_b32_e32 v114, v34
	v_mov_b32_e32 v115, v34
	v_mov_b32_e32 v116, v34
	v_mov_b32_e32 v117, v34
	v_mov_b32_e32 v118, v34
	v_mov_b32_e32 v119, v34
	v_mov_b32_e32 v120, v34
	v_mov_b32_e32 v121, v34
	v_mov_b32_e32 v122, v34
	v_mov_b32_e32 v123, v34
	v_mov_b32_e32 v124, v34
	v_mov_b32_e32 v125, v34
	v_mov_b32_e32 v126, v34
	v_mov_b32_e32 v127, v34
	v_mov_b32_e32 v128, v34
	v_mov_b32_e32 v129, v34
	v_mov_b32_e32 v130, v34
	v_mov_b32_e32 v131, v34
	v_mov_b32_e32 v132, v34
	v_mov_b32_e32 v133, v34
	v_mov_b32_e32 v134, v34
	v_mov_b32_e32 v135, v34
	v_mov_b32_e32 v136, v34
	v_mov_b32_e32 v137, v34
	v_mov_b32_e32 v138, v34
	v_mov_b32_e32 v139, v34
	v_mov_b32_e32 v140, v34
	v_mov_b32_e32 v141, v34
	v_mov_b32_e32 v142, v34
	v_mov_b32_e32 v143, v34
	v_mov_b32_e32 v144, v34
	v_mov_b32_e32 v145, v34
	v_mov_b32_e32 v146, v34
	v_mov_b32_e32 v147, v34
	v_mov_b32_e32 v148, v34
	v_mov_b32_e32 v149, v34
	v_mov_b32_e32 v150, v34
	v_mov_b32_e32 v151, v34
	v_mov_b32_e32 v152, v34
	v_mov_b32_e32 v153, v34
	v_mov_b32_e32 v154, v34
	v_mov_b32_e32 v155, v34
	v_mov_b32_e32 v156, v34
	v_mov_b32_e32 v157, v34
	v_mov_b32_e32 v158, v34
	v_mov_b32_e32 v159, v34
	v_mov_b32_e32 v160, v34
	v_mov_b32_e32 v161, v34

.LBB0_1539:
	s_ashr_i32 s10, s16, 5
	s_ashr_i32 s11, s10, 31
	s_mul_i32 s14, s10, 0x580000
	s_mul_hi_i32 s2, s10, 0x580000
	s_add_u32 s14, s19, s14
	s_addc_u32 s15, s20, s2
	s_mul_i32 s17, s10, 0x1600000
	s_mul_hi_i32 s2, s10, 0x1600000
	s_add_u32 s17, s64, s17
	s_addc_u32 s2, s65, s2
	s_lshl_b32 s30, s16, 6
	s_and_b32 s30, s30, 0x700
	s_lshl_b32 s31, s30, 2
	s_add_u32 s17, s17, s31
	s_addc_u32 s38, s2, 0
	s_lshl_b32 s2, s16, 8
	v_readfirstlane_b32 s16, v0
	s_and_b32 s31, s2, 0x300
	s_lshr_b32 s2, s16, 6
	s_lshl_b32 s34, s2, 9
	s_lshl_b32 s33, s2, 5
	s_and_b32 s35, s33, 0x60
	v_mov_b32_e32 v3, s34
	s_lshr_b32 s34, s16, 1
	v_bitop3_b32 v206, s35, v3, v194 bitop3:0xde
	s_and_b32 s35, s34, 0x7fffff80
	s_lshl_b32 s34, s16, 1
	s_and_b32 s34, s34, 0x180
	s_or_b32 s36, s34, 32
	v_or_b32_e32 v2, s31, v171
	v_bitop3_b32 v181, s36, v201, v198 bitop3:0xde
	s_or_b32 s36, s34, 64
	v_mul_u32_u24_e32 v34, 0xb00, v2
	v_bitop3_b32 v179, s36, v201, v198 bitop3:0xde
	s_or_b32 s36, s34, 0x60
	v_or_b32_e32 v2, v34, v177
	v_bitop3_b32 v172, s36, v201, v198 bitop3:0xde
	s_lshl_b32 s36, s2, 10
	v_lshlrev_b32_e32 v35, 1, v2
	s_add_i32 s36, s36, 0
	s_mov_b32 s37, m0
	s_mov_b32 m0, s36
	s_nop 0
	global_load_lds_dwordx4 v35, s[14:15]
	s_mov_b32 m0, s37
	s_add_i32 s37, s36, 0x2000
	v_add_lshl_u32 v36, v190, v34, 1
	s_mov_b32 s39, m0
	s_mov_b32 m0, s37
	s_nop 0
	global_load_lds_dwordx4 v36, s[14:15]
	s_mov_b32 m0, s39
	s_add_i32 s37, s36, 0x4000
	v_add_lshl_u32 v37, v191, v34, 1
	s_mov_b32 s39, m0
	s_mov_b32 m0, s37
	s_nop 0
	global_load_lds_dwordx4 v37, s[14:15]
	s_mov_b32 m0, s39
	s_add_i32 s37, s36, 0x6000
	s_lshl_b64 s[40:41], s[2:3], 13
	s_add_u32 s40, s17, s40
	v_bitop3_b32 v2, s33, v194, v203 bitop3:0x6c
	v_or_b32_e32 v4, s35, v1
	s_addc_u32 s41, s38, s41
	s_waitcnt vmcnt(1)
	v_add_lshl_u32 v38, v192, v34, 1
	v_lshlrev_b32_e32 v39, 7, v4
	v_bitop3_b32 v205, v2, s23, v3 bitop3:0x36
	s_mov_b32 s39, m0
	s_mov_b32 m0, s37
	s_nop 0
	global_load_lds_dwordx4 v38, s[14:15]
	s_mov_b32 m0, s39
	global_load_dwordx4 v[2:5], v199, s[40:41] nt
	s_add_i32 s40, s2, 8
	s_mov_b32 s41, s3
	s_lshl_b64 s[40:41], s[40:41], 13
	s_add_u32 s40, s17, s40
	s_addc_u32 s41, s38, s41
	global_load_dwordx4 v[6:9], v199, s[40:41] nt
	s_add_i32 s40, s2, 16
	s_mov_b32 s41, s3
	s_lshl_b64 s[40:41], s[40:41], 13
	s_add_u32 s40, s17, s40
	s_addc_u32 s41, s38, s41
	global_load_dwordx4 v[10:13], v199, s[40:41] nt
	s_add_i32 s40, s2, 24
	s_mov_b32 s41, s3
	s_lshl_b64 s[40:41], s[40:41], 13
	s_add_u32 s40, s17, s40
	s_addc_u32 s41, s38, s41
	global_load_dwordx4 v[14:17], v199, s[40:41] nt
	s_add_i32 s40, s2, 32
	s_mov_b32 s41, s3
	s_lshl_b64 s[40:41], s[40:41], 13
	s_add_u32 s40, s17, s40
	s_addc_u32 s41, s38, s41
	global_load_dwordx4 v[18:21], v199, s[40:41] nt
	s_add_i32 s40, s2, 40
	s_mov_b32 s41, s3
	s_lshl_b64 s[40:41], s[40:41], 13
	s_add_u32 s40, s17, s40
	s_addc_u32 s41, s38, s41
	global_load_dwordx4 v[22:25], v199, s[40:41] nt
	s_add_i32 s40, s2, 48
	s_mov_b32 s41, s3
	s_lshl_b64 s[40:41], s[40:41], 13
	s_add_u32 s40, s17, s40
	s_addc_u32 s41, s38, s41
	global_load_dwordx4 v[26:29], v199, s[40:41] nt
	s_add_i32 s40, s2, 56
	s_mov_b32 s41, s3
	s_lshl_b64 s[40:41], s[40:41], 13
	s_add_u32 s40, s17, s40
	s_addc_u32 s41, s38, s41
	s_add_i32 s39, s36, 0x8000
	v_or_b32_e32 v35, 0x80, v35
	global_load_dwordx4 v[30:33], v199, s[40:41] nt
	s_mov_b32 s40, m0
	s_mov_b32 m0, s39
	s_nop 0
	global_load_lds_dwordx4 v35, s[14:15]
	s_mov_b32 m0, s40
	v_or_b32_e32 v35, 0x80, v36
	s_add_i32 s39, s36, 0xa000
	s_mov_b32 s40, m0
	s_mov_b32 m0, s39
	s_nop 0
	global_load_lds_dwordx4 v35, s[14:15]
	s_mov_b32 m0, s40
	v_or_b32_e32 v35, 0x80, v37
	s_add_i32 s39, s36, 0xc000
	s_mov_b32 s40, m0
	s_mov_b32 m0, s39
	s_nop 0
	global_load_lds_dwordx4 v35, s[14:15]
	s_mov_b32 m0, s40
	v_or_b32_e32 v35, 0x80, v38
	s_add_i32 s39, s36, 0xe000
	s_mov_b32 s40, m0
	s_mov_b32 m0, s39
	s_nop 0
	global_load_lds_dwordx4 v35, s[14:15]
	s_mov_b32 m0, s40
	s_waitcnt vmcnt(4)
	s_add_i32 s40, s2, 64
	v_cvt_pk_bf16_f32 v2, v2, v3
	v_cvt_pk_bf16_f32 v3, v4, v5
	v_add_u32_e32 v4, s24, v206
	ds_write_b64 v4, v[2:3]
	v_cvt_pk_bf16_f32 v2, v6, v7
	v_cvt_pk_bf16_f32 v3, v8, v9
	v_add_u32_e32 v5, s24, v205
	ds_write_b64 v5, v[2:3] offset:4096
	v_cvt_pk_bf16_f32 v2, v10, v11
	v_cvt_pk_bf16_f32 v3, v12, v13
	ds_write_b64 v4, v[2:3] offset:8192
	v_cvt_pk_bf16_f32 v2, v14, v15
	v_cvt_pk_bf16_f32 v3, v16, v17
	ds_write_b64 v5, v[2:3] offset:12288
	v_cvt_pk_bf16_f32 v2, v18, v19
	v_cvt_pk_bf16_f32 v3, v20, v21
	s_mov_b32 s41, s3
	ds_write_b64 v4, v[2:3] offset:16384
	v_cvt_pk_bf16_f32 v2, v22, v23
	v_cvt_pk_bf16_f32 v3, v24, v25
	s_lshl_b64 s[40:41], s[40:41], 13
	ds_write_b64 v5, v[2:3] offset:20480
	v_cvt_pk_bf16_f32 v2, v26, v27
	v_cvt_pk_bf16_f32 v3, v28, v29
	s_add_u32 s40, s17, s40
	ds_write_b64 v4, v[2:3] offset:24576
	v_cvt_pk_bf16_f32 v2, v30, v31
	v_cvt_pk_bf16_f32 v3, v32, v33
	s_addc_u32 s41, s38, s41
	ds_write_b64 v5, v[2:3] offset:28672
	global_load_dwordx4 v[30:33], v199, s[40:41] nt
	s_add_i32 s40, s2, 0x48
	s_mov_b32 s41, s3
	s_lshl_b64 s[40:41], s[40:41], 13
	s_add_u32 s40, s17, s40
	s_addc_u32 s41, s38, s41
	global_load_dwordx4 v[26:29], v199, s[40:41] nt
	s_add_i32 s40, s2, 0x50
	s_mov_b32 s41, s3
	s_lshl_b64 s[40:41], s[40:41], 13
	s_add_u32 s40, s17, s40
	s_addc_u32 s41, s38, s41
	global_load_dwordx4 v[22:25], v199, s[40:41] nt
	s_add_i32 s40, s2, 0x58
	s_mov_b32 s41, s3
	s_lshl_b64 s[40:41], s[40:41], 13
	s_add_u32 s40, s17, s40
	s_addc_u32 s41, s38, s41
	global_load_dwordx4 v[18:21], v199, s[40:41] nt
	s_add_i32 s40, s2, 0x60
	s_mov_b32 s41, s3
	s_lshl_b64 s[40:41], s[40:41], 13
	s_add_u32 s40, s17, s40
	s_addc_u32 s41, s38, s41
	global_load_dwordx4 v[14:17], v199, s[40:41] nt
	s_add_i32 s40, s2, 0x68
	s_mov_b32 s41, s3
	s_lshl_b64 s[40:41], s[40:41], 13
	s_add_u32 s40, s17, s40
	s_addc_u32 s41, s38, s41
	global_load_dwordx4 v[10:13], v199, s[40:41] nt
	s_add_i32 s40, s2, 0x70
	s_mov_b32 s41, s3
	s_lshl_b64 s[40:41], s[40:41], 13
	s_add_u32 s40, s17, s40
	s_addc_u32 s41, s38, s41
	s_addk_i32 s2, 0x78
	global_load_dwordx4 v[6:9], v199, s[40:41] nt
	s_lshl_b64 s[40:41], s[2:3], 13
	s_add_u32 s40, s17, s40
	s_addc_u32 s41, s38, s41
	global_load_dwordx4 v[2:5], v199, s[40:41] nt
	s_lshl_b64 s[40:41], s[16:17], 7
	s_waitcnt lgkmcnt(0)
	s_barrier
	s_and_b32 s16, s41, 0x7f
	s_and_b32 s2, s40, 0xffffe000
	s_add_u32 s2, s17, s2
	v_lshl_add_u32 v209, v34, 1, v202
	v_mov_b32_e32 v34, 0
	v_bitop3_b32 v183, s34, v201, v198 bitop3:0xde
	v_or_b32_e32 v207, v39, v196
	s_mov_b32 s37, 0x8000
	v_or_b32_e32 v208, v39, v197
	s_addc_u32 s38, s38, s16
	s_mov_b32 s39, 0x10000
	s_mov_b32 s40, 0
	s_mov_b64 s[16:17], 0
	v_mov_b32_e32 v35, v34
	v_mov_b32_e32 v36, v34
	v_mov_b32_e32 v37, v34
	v_mov_b32_e32 v38, v34
	v_mov_b32_e32 v39, v34
	v_mov_b32_e32 v40, v34
	v_mov_b32_e32 v41, v34
	s_waitcnt vmcnt(12)
	v_mov_b32_e32 v42, v34
	v_mov_b32_e32 v43, v34
	v_mov_b32_e32 v44, v34
	v_mov_b32_e32 v45, v34
	v_mov_b32_e32 v46, v34
	v_mov_b32_e32 v47, v34
	v_mov_b32_e32 v48, v34
	v_mov_b32_e32 v49, v34
	v_mov_b32_e32 v50, v34
	v_mov_b32_e32 v51, v34
	v_mov_b32_e32 v52, v34
	v_mov_b32_e32 v53, v34
	v_mov_b32_e32 v54, v34
	v_mov_b32_e32 v55, v34
	v_mov_b32_e32 v56, v34
	v_mov_b32_e32 v57, v34
	v_mov_b32_e32 v58, v34
	v_mov_b32_e32 v59, v34
	v_mov_b32_e32 v60, v34
	v_mov_b32_e32 v61, v34
	v_mov_b32_e32 v62, v34
	v_mov_b32_e32 v63, v34
	v_mov_b32_e32 v64, v34
	v_mov_b32_e32 v65, v34
	v_mov_b32_e32 v66, v34
	v_mov_b32_e32 v67, v34
	v_mov_b32_e32 v68, v34
	v_mov_b32_e32 v69, v34
	v_mov_b32_e32 v70, v34
	v_mov_b32_e32 v71, v34
	v_mov_b32_e32 v72, v34
	v_mov_b32_e32 v73, v34
	v_mov_b32_e32 v74, v34
	v_mov_b32_e32 v75, v34
	v_mov_b32_e32 v76, v34
	v_mov_b32_e32 v77, v34
	v_mov_b32_e32 v78, v34
	v_mov_b32_e32 v79, v34
	v_mov_b32_e32 v80, v34
	v_mov_b32_e32 v81, v34
	v_mov_b32_e32 v82, v34
	v_mov_b32_e32 v83, v34
	v_mov_b32_e32 v84, v34
	v_mov_b32_e32 v85, v34
	v_mov_b32_e32 v86, v34
	v_mov_b32_e32 v87, v34
	v_mov_b32_e32 v88, v34
	v_mov_b32_e32 v89, v34
	v_mov_b32_e32 v90, v34
	v_mov_b32_e32 v91, v34
	v_mov_b32_e32 v92, v34
	v_mov_b32_e32 v93, v34
	v_mov_b32_e32 v94, v34
	v_mov_b32_e32 v95, v34
	v_mov_b32_e32 v96, v34
	v_mov_b32_e32 v97, v34
	v_mov_b32_e32 v98, v34
	v_mov_b32_e32 v99, v34
	v_mov_b32_e32 v100, v34
	v_mov_b32_e32 v101, v34
	v_mov_b32_e32 v102, v34
	v_mov_b32_e32 v103, v34
	v_mov_b32_e32 v104, v34
	v_mov_b32_e32 v105, v34
	v_mov_b32_e32 v106, v34
	v_mov_b32_e32 v107, v34
	v_mov_b32_e32 v108, v34
	v_mov_b32_e32 v109, v34
	v_mov_b32_e32 v110, v34
	v_mov_b32_e32 v111, v34
	v_mov_b32_e32 v112, v34
	v_mov_b32_e32 v113, v34
	v_mov_b32_e32 v114, v34
	v_mov_b32_e32 v115, v34
	v_mov_b32_e32 v116, v34
	v_mov_b32_e32 v117, v34
	v_mov_b32_e32 v118, v34
	v_mov_b32_e32 v119, v34
	v_mov_b32_e32 v120, v34
	v_mov_b32_e32 v121, v34
	v_mov_b32_e32 v122, v34
	v_mov_b32_e32 v123, v34
	v_mov_b32_e32 v124, v34
	v_mov_b32_e32 v125, v34
	v_mov_b32_e32 v126, v34
	v_mov_b32_e32 v127, v34
	v_mov_b32_e32 v128, v34
	v_mov_b32_e32 v129, v34
	v_mov_b32_e32 v130, v34
	v_mov_b32_e32 v131, v34
	v_mov_b32_e32 v132, v34
	v_mov_b32_e32 v133, v34
	v_mov_b32_e32 v134, v34
	v_mov_b32_e32 v135, v34
	v_mov_b32_e32 v136, v34
	v_mov_b32_e32 v137, v34
	v_mov_b32_e32 v138, v34
	v_mov_b32_e32 v139, v34
	v_mov_b32_e32 v140, v34
	v_mov_b32_e32 v141, v34
	v_mov_b32_e32 v142, v34
	v_mov_b32_e32 v143, v34
	v_mov_b32_e32 v144, v34
	v_mov_b32_e32 v145, v34
	v_mov_b32_e32 v146, v34
	v_mov_b32_e32 v147, v34
	v_mov_b32_e32 v148, v34
	v_mov_b32_e32 v149, v34
	v_mov_b32_e32 v150, v34
	v_mov_b32_e32 v151, v34
	v_mov_b32_e32 v152, v34
	v_mov_b32_e32 v153, v34
	v_mov_b32_e32 v158, v34
	v_mov_b32_e32 v159, v34
	v_mov_b32_e32 v160, v34
	v_mov_b32_e32 v161, v34
	v_mov_b32_e32 v154, v34
	v_mov_b32_e32 v155, v34
	v_mov_b32_e32 v156, v34
	v_mov_b32_e32 v157, v34
